# speedup vs baseline: 1.0346x; 1.0346x over previous
_Z16sum_layer_kernelPKfS0_Pf:
	s_load_dwordx4 s[4:7], s[0:1], 0x0
	s_load_dwordx2 s[8:9], s[0:1], 0x10
	v_and_b32_e32 v40, 31, v0
	v_bfe_u32 v41, v0, 5, 1
	v_lshrrev_b32_e32 v42, 6, v0
	v_and_b32_e32 v43, 7, v0
	v_bfe_u32 v44, v0, 3, 3
	v_and_b32_e32 v45, 63, v0
	s_lshl_b32 s3, s2, 12
	s_lshl_b32 s19, s2, 7
	v_lshlrev_b32_e32 v1, 11, v41
	v_lshl_or_b32 v1, v40, 2, v1
	v_lshlrev_b32_e32 v46, 4, v43
	v_lshl_add_u32 v35, v44, 16, v46
	v_lshl_add_u32 v35, v42, 21, v35
	v_add_u32_e32 v35, s19, v35
	v_lshlrev_b32_e32 v36, 2, v40
	v_lshl_add_u32 v36, v41, 18, v36
	v_lshl_add_u32 v36, v42, 21, v36
	v_add_u32_e32 v36, s19, v36
	v_mul_u32_u24_e32 v37, 0x1200, v42
	v_mul_u32_u24_e32 v38, 0x90, v44
	v_add3_u32 v38, v37, v38, v46
	v_mul_u32_u24_e32 v39, 0x90, v40
	v_lshlrev_b32_e32 v47, 6, v41
	v_add3_u32 v39, v37, v39, v47
	v_cmp_gt_u32_e32 vcc, 32, v45
	v_mov_b32_e32 v34, 0xc1600000
	s_mov_b32 s16, 0x3fb8aa3b
	s_mov_b32 s17, 0x3f317218
	s_mov_b32 s20, 0x80000
	s_mov_b32 s21, 0x100000
	s_mov_b32 s22, 0x180000
	s_lshl_b32 s24, 1, 16
	s_lshl_b32 s25, 2, 16
	s_lshl_b32 s26, 3, 16
	s_lshl_b32 s27, 8, 16
	s_lshl_b32 s28, 9, 16
	s_lshl_b32 s29, 10, 16
	s_lshl_b32 s30, 11, 16
	s_lshl_b32 s31, 16, 16
	s_lshl_b32 s32, 17, 16
	s_lshl_b32 s33, 18, 16
	s_lshl_b32 s34, 19, 16
	s_lshl_b32 s35, 24, 16
	s_lshl_b32 s36, 25, 16
	s_lshl_b32 s37, 26, 16
	s_lshl_b32 s38, 27, 16
	s_mov_b32 s14, 0x200000
	s_mov_b32 s15, 0x20000
	s_waitcnt lgkmcnt(0)
	s_mov_b32 s12, s6
	s_and_b32 s13, s7, 0xffff
	s_and_b32 s5, s5, 0xffff
	s_mov_b32 s6, 0x800000
	s_mov_b32 s7, s15
	s_and_b32 s9, s9, 0xffff
	s_mov_b32 s10, s6
	s_mov_b32 s11, s15
	buffer_load_dword v18, v1, s[12:15], s3 offen nt
	buffer_load_dword v19, v1, s[12:15], s3 offen offset:128 nt
	buffer_load_dword v20, v1, s[12:15], s3 offen offset:256 nt
	buffer_load_dword v21, v1, s[12:15], s3 offen offset:384 nt
	buffer_load_dword v22, v1, s[12:15], s3 offen offset:512 nt
	buffer_load_dword v23, v1, s[12:15], s3 offen offset:640 nt
	buffer_load_dword v24, v1, s[12:15], s3 offen offset:768 nt
	buffer_load_dword v25, v1, s[12:15], s3 offen offset:896 nt
	buffer_load_dword v26, v1, s[12:15], s3 offen offset:1024 nt
	buffer_load_dword v27, v1, s[12:15], s3 offen offset:1152 nt
	buffer_load_dword v28, v1, s[12:15], s3 offen offset:1280 nt
	buffer_load_dword v29, v1, s[12:15], s3 offen offset:1408 nt
	buffer_load_dword v30, v1, s[12:15], s3 offen offset:1536 nt
	buffer_load_dword v31, v1, s[12:15], s3 offen offset:1664 nt
	buffer_load_dword v32, v1, s[12:15], s3 offen offset:1792 nt
	buffer_load_dword v33, v1, s[12:15], s3 offen offset:1920 nt
	buffer_load_dwordx4 v[2:5], v35, s[4:7], 0 offen nt
	buffer_load_dwordx4 v[6:9], v35, s[4:7], s20 offen nt
	buffer_load_dwordx4 v[10:13], v35, s[4:7], s21 offen nt
	buffer_load_dwordx4 v[14:17], v35, s[4:7], s22 offen nt
	s_waitcnt vmcnt(4)
	v_max3_f32 v49, v18, v19, v20
	v_max3_f32 v50, v21, v22, v23
	v_max3_f32 v49, v49, v24, v25
	v_max3_f32 v50, v50, v26, v27
	v_max3_f32 v49, v49, v28, v29
	v_max3_f32 v50, v50, v30, v31
	v_max3_f32 v49, v49, v32, v33
	v_max_f32_e32 v49, v49, v50
	v_mov_b32_e32 v50, v49
	s_nop 1
	v_permlane32_swap_b32_e32 v49, v50
	v_max_f32_e32 v49, v49, v50
	v_fmamk_f32 v49, v49, 0x3fb8aa3b, v34
	v_fma_f32 v18, v18, s16, -v49
	v_exp_f32_e32 v18, v18
	v_fma_f32 v19, v19, s16, -v49
	v_exp_f32_e32 v19, v19
	v_fma_f32 v20, v20, s16, -v49
	v_exp_f32_e32 v20, v20
	v_fma_f32 v21, v21, s16, -v49
	v_exp_f32_e32 v21, v21
	v_fma_f32 v22, v22, s16, -v49
	v_exp_f32_e32 v22, v22
	v_fma_f32 v23, v23, s16, -v49
	v_exp_f32_e32 v23, v23
	v_fma_f32 v24, v24, s16, -v49
	v_exp_f32_e32 v24, v24
	v_fma_f32 v25, v25, s16, -v49
	v_exp_f32_e32 v25, v25
	v_fma_f32 v26, v26, s16, -v49
	v_exp_f32_e32 v26, v26
	v_fma_f32 v27, v27, s16, -v49
	v_exp_f32_e32 v27, v27
	v_fma_f32 v28, v28, s16, -v49
	v_exp_f32_e32 v28, v28
	v_fma_f32 v29, v29, s16, -v49
	v_exp_f32_e32 v29, v29
	v_fma_f32 v30, v30, s16, -v49
	v_exp_f32_e32 v30, v30
	v_fma_f32 v31, v31, s16, -v49
	v_exp_f32_e32 v31, v31
	v_fma_f32 v32, v32, s16, -v49
	v_exp_f32_e32 v32, v32
	v_fma_f32 v33, v33, s16, -v49
	v_exp_f32_e32 v33, v33
	v_add_f32_e32 v50, v18, v19
	v_add_f32_e32 v51, v20, v21
	v_add_f32_e32 v50, v50, v22
	v_add_f32_e32 v51, v51, v23
	v_add_f32_e32 v50, v50, v24
	v_add_f32_e32 v51, v51, v25
	v_add_f32_e32 v50, v50, v26
	v_add_f32_e32 v51, v51, v27
	v_add_f32_e32 v50, v50, v28
	v_add_f32_e32 v51, v51, v29
	v_add_f32_e32 v50, v50, v30
	v_add_f32_e32 v51, v51, v31
	v_add_f32_e32 v50, v50, v32
	v_add_f32_e32 v51, v51, v33
	v_add_f32_e32 v50, v50, v51
	v_mov_b32_e32 v51, v50
	s_nop 1
	v_permlane32_swap_b32_e32 v50, v51
	v_add_f32_e32 v50, v50, v51
	v_log_f32_e32 v50, v50
	v_cvt_pk_f16_f32 v40, v18, v19
	v_cvt_pk_f16_f32 v41, v20, v21
	v_cvt_pk_f16_f32 v42, v22, v23
	v_cvt_pk_f16_f32 v43, v24, v25
	v_cvt_pk_f16_f32 v44, v26, v27
	v_cvt_pk_f16_f32 v45, v28, v29
	v_cvt_pk_f16_f32 v46, v30, v31
	v_cvt_pk_f16_f32 v47, v32, v33
	v_add_f32_e32 v50, 0x41600000, v50
	v_mul_f32_e32 v50, 0xbf317218, v50
	v_cndmask_b32_e64 v51, v50, 1.0, vcc
	s_waitcnt vmcnt(3)
	ds_write_b128 v38, v[2:5]
	s_waitcnt vmcnt(2)
	ds_write_b128 v38, v[6:9] offset:1152
	s_waitcnt vmcnt(1)
	ds_write_b128 v38, v[10:13] offset:2304
	s_waitcnt vmcnt(0)
	ds_write_b128 v38, v[14:17] offset:3456
	ds_read_b128 v[2:5], v39
	ds_read_b128 v[6:9], v39 offset:16
	ds_read_b128 v[10:13], v39 offset:32
	ds_read_b128 v[14:17], v39 offset:48
	s_waitcnt lgkmcnt(2)
	v_max3_f32 v52, v2, v3, v4
	v_max3_f32 v53, v5, v6, v7
	v_max_f32_e32 v52, v52, v8
	v_max_f32_e32 v53, v53, v9
	s_waitcnt lgkmcnt(0)
	v_max3_f32 v52, v52, v10, v11
	v_max3_f32 v53, v53, v12, v13
	v_max3_f32 v52, v52, v14, v15
	v_max3_f32 v53, v53, v16, v17
	v_max_f32_e32 v52, v52, v53
	v_mov_b32_e32 v53, v52
	s_nop 1
	v_permlane32_swap_b32_e32 v52, v53
	v_max_f32_e32 v52, v52, v53
	v_cndmask_b32_e32 v54, 1.0, v52, vcc
	v_fmamk_f32 v55, v52, 0x3fb8aa3b, v34
	v_fma_f32 v2, v2, s16, -v55
	v_mfma_f32_32x32x2_f32 v[64:79], v54, v51, 0
	v_exp_f32_e32 v2, v2
	v_fma_f32 v3, v3, s16, -v55
	v_exp_f32_e32 v3, v3
	v_fma_f32 v4, v4, s16, -v55
	v_exp_f32_e32 v4, v4
	v_fma_f32 v5, v5, s16, -v55
	v_exp_f32_e32 v5, v5
	v_fma_f32 v6, v6, s16, -v55
	v_exp_f32_e32 v6, v6
	v_fma_f32 v7, v7, s16, -v55
	v_exp_f32_e32 v7, v7
	v_fma_f32 v8, v8, s16, -v55
	v_exp_f32_e32 v8, v8
	v_fma_f32 v9, v9, s16, -v55
	v_exp_f32_e32 v9, v9
	v_fma_f32 v10, v10, s16, -v55
	v_exp_f32_e32 v10, v10
	v_cvt_pk_f16_f32 v56, v2, v3
	v_cvt_pk_f16_f32 v57, v4, v5
	v_cvt_pk_f16_f32 v58, v6, v7
	v_cvt_pk_f16_f32 v59, v8, v9
	v_fma_f32 v11, v11, s16, -v55
	v_exp_f32_e32 v11, v11
	v_fma_f32 v12, v12, s16, -v55
	v_exp_f32_e32 v12, v12
	v_mfma_f32_32x32x16_f16 v[18:33], v[56:59], v[40:43], 0
	v_fma_f32 v13, v13, s16, -v55
	v_exp_f32_e32 v13, v13
	v_fma_f32 v14, v14, s16, -v55
	v_exp_f32_e32 v14, v14
	v_fma_f32 v15, v15, s16, -v55
	v_exp_f32_e32 v15, v15
	v_fma_f32 v16, v16, s16, -v55
	v_exp_f32_e32 v16, v16
	v_fma_f32 v17, v17, s16, -v55
	v_exp_f32_e32 v17, v17
	v_cvt_pk_f16_f32 v60, v10, v11
	v_cvt_pk_f16_f32 v61, v12, v13
	v_cvt_pk_f16_f32 v62, v14, v15
	v_cvt_pk_f16_f32 v63, v16, v17
	s_nop 1
	v_mfma_f32_32x32x16_f16 v[18:33], v[60:63], v[44:47], v[18:33]
	s_nop 11
	v_log_f32_e32 v18, v18
	v_log_f32_e32 v19, v19
	v_log_f32_e32 v20, v20
	v_fmac_f32_e32 v64, s17, v18
	buffer_store_dword v64, v36, s[8:11], 0 offen
	v_log_f32_e32 v21, v21
	v_fmac_f32_e32 v65, s17, v19
	buffer_store_dword v65, v36, s[8:11], s24 offen
	v_log_f32_e32 v22, v22
	v_fmac_f32_e32 v66, s17, v20
	buffer_store_dword v66, v36, s[8:11], s25 offen
	v_log_f32_e32 v23, v23
	v_fmac_f32_e32 v67, s17, v21
	buffer_store_dword v67, v36, s[8:11], s26 offen
	v_log_f32_e32 v24, v24
	v_fmac_f32_e32 v68, s17, v22
	buffer_store_dword v68, v36, s[8:11], s27 offen
	v_log_f32_e32 v25, v25
	v_fmac_f32_e32 v69, s17, v23
	buffer_store_dword v69, v36, s[8:11], s28 offen
	v_log_f32_e32 v26, v26
	v_fmac_f32_e32 v70, s17, v24
	buffer_store_dword v70, v36, s[8:11], s29 offen
	v_log_f32_e32 v27, v27
	v_fmac_f32_e32 v71, s17, v25
	buffer_store_dword v71, v36, s[8:11], s30 offen
	v_log_f32_e32 v28, v28
	v_fmac_f32_e32 v72, s17, v26
	buffer_store_dword v72, v36, s[8:11], s31 offen
	v_log_f32_e32 v29, v29
	v_fmac_f32_e32 v73, s17, v27
	buffer_store_dword v73, v36, s[8:11], s32 offen
	v_log_f32_e32 v30, v30
	v_fmac_f32_e32 v74, s17, v28
	buffer_store_dword v74, v36, s[8:11], s33 offen
	v_log_f32_e32 v31, v31
	v_fmac_f32_e32 v75, s17, v29
	buffer_store_dword v75, v36, s[8:11], s34 offen
	v_log_f32_e32 v32, v32
	v_fmac_f32_e32 v76, s17, v30
	buffer_store_dword v76, v36, s[8:11], s35 offen
	v_log_f32_e32 v33, v33
	v_fmac_f32_e32 v77, s17, v31
	buffer_store_dword v77, v36, s[8:11], s36 offen
	v_fmac_f32_e32 v78, s17, v32
	buffer_store_dword v78, v36, s[8:11], s37 offen
	v_fmac_f32_e32 v79, s17, v33
	buffer_store_dword v79, v36, s[8:11], s38 offen
	s_endpgm

	.amdhsa_kernel _Z16sum_layer_kernelPKfS0_Pf
		.amdhsa_group_segment_fixed_size 18432
		.amdhsa_private_segment_fixed_size 0
		.amdhsa_kernarg_size 24
		.amdhsa_user_sgpr_count 2
		.amdhsa_user_sgpr_dispatch_ptr 0
		.amdhsa_user_sgpr_queue_ptr 0
		.amdhsa_user_sgpr_kernarg_segment_ptr 1
		.amdhsa_user_sgpr_dispatch_id 0
		.amdhsa_user_sgpr_kernarg_preload_length 0
		.amdhsa_user_sgpr_kernarg_preload_offset 0
		.amdhsa_user_sgpr_private_segment_size 0
		.amdhsa_uses_dynamic_stack 0
		.amdhsa_enable_private_segment 0
		.amdhsa_system_sgpr_workgroup_id_x 1
		.amdhsa_system_sgpr_workgroup_id_y 0
		.amdhsa_system_sgpr_workgroup_id_z 0
		.amdhsa_system_sgpr_workgroup_info 0
		.amdhsa_system_vgpr_workitem_id 0
		.amdhsa_next_free_vgpr 80
		.amdhsa_next_free_sgpr 39
		.amdhsa_accum_offset 80
		.amdhsa_reserve_vcc 1
		.amdhsa_float_round_mode_32 0
		.amdhsa_float_round_mode_16_64 0
		.amdhsa_float_denorm_mode_32 3
		.amdhsa_float_denorm_mode_16_64 3
		.amdhsa_dx10_clamp 1
		.amdhsa_ieee_mode 1
		.amdhsa_fp16_overflow 0
		.amdhsa_tg_split 0
		.amdhsa_exception_fp_ieee_invalid_op 0
		.amdhsa_exception_fp_denorm_src 0
		.amdhsa_exception_fp_ieee_div_zero 0
		.amdhsa_exception_fp_ieee_overflow 0
		.amdhsa_exception_fp_ieee_underflow 0
		.amdhsa_exception_fp_ieee_inexact 0
		.amdhsa_exception_int_div_zero 0
	.end_amdhsa_kernel

amdhsa.kernels:
  - .agpr_count:     0
    .args:
      - .address_space:  global
        .offset:         0
        .size:           8
        .value_kind:     global_buffer
      - .address_space:  global
        .offset:         8
        .size:           8
        .value_kind:     global_buffer
      - .address_space:  global
        .offset:         16
        .size:           8
        .value_kind:     global_buffer
    .group_segment_fixed_size: 18432
    .kernarg_segment_align: 8
    .kernarg_segment_size: 24
    .language:       OpenCL C
    .language_version:
      - 2
      - 0
    .max_flat_workgroup_size: 256
    .name:           _Z16sum_layer_kernelPKfS0_Pf
    .private_segment_fixed_size: 0
    .sgpr_count:     45
    .sgpr_spill_count: 0
    .symbol:         _Z16sum_layer_kernelPKfS0_Pf.kd
    .uniform_work_group_size: 1
    .uses_dynamic_stack: false
    .vgpr_count:     80
    .vgpr_spill_count: 0
    .wavefront_size: 64
